# S1 + static s_setprio 1 for waves 4-7 during the attention phase
# baseline (speedup 1.0000x reference)
.LBB0_613:
	v_readlane_b32 s16, v253, 6
	v_readlane_b32 s18, v253, 8
	v_readlane_b32 s17, v253, 7
	s_cmp_le_i32 s18, s2
	s_cselect_b64 s[16:17], -1, 0
	s_and_b64 s[0:1], s[16:17], s[20:21]
	s_andn2_b64 vcc, exec, s[0:1]
	v_readlane_b32 s19, v253, 9
	s_cbranch_vccnz .LBB0_683
	v_readlane_b32 s0, v253, 2
	v_readlane_b32 s1, v253, 3
	s_load_dwordx2 s[0:1], s[0:1], 0xf8
	v_readlane_b32 s2, v255, 1
	v_readlane_b32 s3, v255, 2
	s_andn2_b64 vcc, exec, s[2:3]
	s_cbranch_vccnz .LBB0_669
	s_waitcnt lgkmcnt(0)
	s_add_u32 s2, s0, 0x45901800
	s_addc_u32 s3, s1, 0
	s_add_u32 s13, s0, 0x45902000
	s_addc_u32 s18, s1, 0
	s_add_u32 s19, s0, 0x45902200
	s_addc_u32 s27, s1, 0
	s_add_u32 s28, s0, 0x45a12000
	s_addc_u32 s29, s1, 0
	s_add_u32 s30, s0, 0x45a12200
	s_addc_u32 s31, s1, 0
	s_add_u32 s34, s0, 0x475b2000
	v_readlane_b32 s37, v254, 63
	s_addc_u32 s35, s1, 0
	s_mov_b32 s36, s37
	s_cmp_ge_u32 s33, 0x100
	s_cbranch_scc0 .Lattn_noprio
	s_setprio 1
.Lattn_noprio:
	s_branch .LBB0_617
.LBB0_616:
	s_add_i32 s37, s37, s90
	s_add_i32 s36, s36, s90
	s_cmpk_gt_i32 s37, 0xff
	s_cbranch_scc1 .LBB0_669

.LBB0_669:
	s_setprio 0
	v_readlane_b32 s2, v254, 32
	v_readlane_b32 s3, v254, 33
	v_readlane_b32 s68, v255, 43
	s_waitcnt lgkmcnt(0)
	s_barrier
	v_mbcnt_lo_u32_b32 v0, -1, 0
	v_mbcnt_hi_u32_b32 v0, -1, v0
	s_andn2_b64 vcc, exec, s[2:3]
	v_or_b32_e32 v132, s33, v0
	v_readlane_b32 s66, v255, 41
	s_mov_b32 s35, 0xff61b1e6
	s_mov_b32 s37, 0x3fb8aa3b
	s_mov_b32 s65, 0xc2ce8ed0
	s_mov_b32 s70, 0x42b17218
	v_readlane_b32 s69, v255, 44
	v_readlane_b32 s67, v255, 42
	s_cbranch_vccnz .LBB0_683
	s_waitcnt vmcnt(0)
	v_bfe_u32 v3, v132, 3, 1
	v_bfe_u32 v1, v132, 4, 2
	v_lshlrev_b32_e32 v2, 2, v132
	v_xor_b32_e32 v3, 0xff, v3
	v_and_b32_e32 v134, 0xffffff00, v2
	v_bitop3_b32 v2, v132, 7, v132 bitop3:0xc
	v_add_lshl_u32 v3, v3, v1, 4
	s_movk_i32 s9, 0x2040
	v_mad_u32_u24 v3, v2, s9, v3
	v_add_u32_e32 v2, 0, v3
	v_lshlrev_b32_e32 v4, 1, v134
	v_sub_u32_e32 v142, v2, v4
	v_add_u32_e32 v4, 0x200, v132
	v_lshrrev_b32_e32 v4, 8, v4
	v_mul_i32_i24_e32 v10, 0x1010, v4
	v_add_u32_e32 v4, 0x400, v132
	v_lshrrev_b32_e32 v4, 8, v4
	v_mul_i32_i24_e32 v11, 0x1010, v4
	v_add_u32_e32 v4, 0x600, v132
	v_lshrrev_b32_e32 v4, 8, v4
	v_mul_i32_i24_e32 v12, 0x1010, v4
	v_add_u32_e32 v4, 0x800, v132
	v_lshrrev_b32_e32 v4, 8, v4
	s_lshl_b32 s2, s84, 22
	v_mul_i32_i24_e32 v13, 0x1010, v4
	v_add_u32_e32 v4, 0xa00, v132
	s_add_u32 s2, s0, s2
	v_readlane_b32 s10, v255, 23
	v_lshrrev_b32_e32 v4, 8, v4
	v_and_b32_e32 v0, 15, v132
	s_addc_u32 s3, s1, 0
	v_mov_b32_e32 v2, s10
	s_movk_i32 s9, 0x1010
	v_mul_i32_i24_e32 v14, 0x1010, v4
	v_add_u32_e32 v4, 0xc00, v132
	s_add_u32 s13, s0, 0x6b900000
	v_mad_u32_u24 v7, v0, s9, v2
	s_movk_i32 s9, 0x1008
	v_lshrrev_b32_e32 v4, 8, v4
	s_addc_u32 s18, s1, 0
	v_cmp_gt_i32_e64 s[42:43], s9, v132
	v_lshlrev_b32_e32 v143, 4, v132
	v_mul_i32_i24_e32 v15, 0x1010, v4
	v_add_u32_e32 v4, 0xe00, v132
	v_readlane_b32 s9, v255, 16
	v_and_b32_e32 v2, 0xff0, v143
	v_ashrrev_i32_e32 v133, 31, v132
	v_lshrrev_b32_e32 v4, 8, v4
	s_add_u32 s0, s0, s9
	v_readlane_b32 s9, v255, 17
	s_mov_b32 s85, s73
	v_add_u32_e32 v9, s10, v2
	v_mul_i32_i24_e32 v16, 0x1010, v4
	s_addc_u32 s1, s1, s9
	s_lshl_b64 s[10:11], s[84:85], 22
	v_lshlrev_b64 v[4:5], 1, v[132:133]
	v_mov_b32_e32 v17, s11
	v_sub_co_u32_e32 v4, vcc, s10, v4
	v_lshlrev_b32_e32 v8, 4, v1
	s_nop 0
	v_subb_co_u32_e32 v5, vcc, v17, v5, vcc
	v_lshl_add_u64 v[136:137], s[0:1], 0, v[4:5]
	v_lshlrev_b32_e32 v4, 3, v132
	v_lshlrev_b32_e32 v2, 2, v1
	v_lshrrev_b32_e32 v1, 8, v132
	v_and_b32_e32 v4, 0xfffffe00, v4
	v_mul_u32_u24_e32 v6, 0x1010, v0
	v_lshlrev_b32_e32 v0, 11, v0
	v_mul_i32_i24_e32 v1, 0x1010, v1
	v_readlane_b32 s0, v255, 24
	v_sub_u32_e32 v3, v3, v4
	v_ashrrev_i32_e32 v135, 31, v134
	v_subrev_u32_e32 v144, 32, v142
	v_subrev_u32_e32 v145, 64, v142
	v_add_u32_e32 v146, 0xffffffa0, v142
	v_add_u32_e32 v147, 0xffffff80, v142
	v_add_u32_e32 v148, 0xffffff60, v142
	v_add_u32_e32 v149, 0xffffff40, v142
	v_add_u32_e32 v150, 0xffffff20, v142
	v_add_u32_e32 v151, 0xffffff00, v142
	v_add_u32_e32 v152, 0xfffffee0, v142
	v_add_u32_e32 v153, 0xfffffec0, v142
	v_add_u32_e32 v154, 0xfffffea0, v142
	v_add_u32_e32 v155, 0xfffffe80, v142
	v_add_u32_e32 v156, 0xfffffe60, v142
	v_add_u32_e32 v157, 0xfffffe40, v142
	v_add_u32_e32 v158, 0xfffffe20, v142
	v_lshl_add_u32 v159, v132, 1, s0
	v_add3_u32 v160, 0, 32, v3
	v_add3_u32 v161, v6, v8, 0
	v_add_u32_e32 v162, v9, v1
	v_add_u32_e32 v163, v9, v10
	v_add_u32_e32 v164, v9, v11
	v_add_u32_e32 v165, v9, v12
	v_add_u32_e32 v166, v9, v13
	v_add_u32_e32 v167, v9, v14
	v_add_u32_e32 v168, v9, v15
	v_add_u32_e32 v169, v9, v16
	v_lshlrev_b32_e32 v138, 1, v0
	v_lshlrev_b32_e32 v140, 1, v2
	v_add_u32_e32 v170, v7, v8
	v_readlane_b32 s0, v255, 14
	v_readlane_b32 s1, v255, 15
